# in-projection phase: 210 GEMM workgroups / 46 conversion workgroups (15 whole GEMM rounds) with the new conversion queue
# baseline (speedup 1.0000x reference)
.LBB0_74:
	s_load_dwordx16 s[8:23], s[0:1], 0x40
	v_writelane_b32 v254, s34, 10
	s_cmp_lt_i32 s30, 2
	s_cselect_b64 s[0:1], -1, 0
	v_writelane_b32 v254, s35, 11
	s_waitcnt lgkmcnt(0)
	v_writelane_b32 v254, s8, 12
	s_add_u32 s2, s28, 0x3300000
	s_addc_u32 s3, s29, 0
	v_writelane_b32 v254, s9, 13
	v_writelane_b32 v254, s10, 14
	v_writelane_b32 v254, s11, 15
	v_writelane_b32 v254, s12, 16
	v_writelane_b32 v254, s13, 17
	v_writelane_b32 v254, s14, 18
	v_writelane_b32 v254, s15, 19
	v_writelane_b32 v254, s16, 20
	v_writelane_b32 v254, s17, 21
	v_writelane_b32 v254, s18, 22
	v_writelane_b32 v254, s19, 23
	v_writelane_b32 v254, s20, 24
	v_writelane_b32 v254, s21, 25
	v_writelane_b32 v254, s22, 26
	v_writelane_b32 v254, s23, 27
	v_writelane_b32 v254, s2, 28
	s_nop 1
	v_writelane_b32 v254, s3, 29
	s_add_u32 s2, s28, 0x4300000
	s_addc_u32 s3, s29, 0
	v_writelane_b32 v254, s2, 30
	s_nop 1
	v_writelane_b32 v254, s3, 31
	s_add_u32 s2, s28, 0x5b00000
	s_addc_u32 s3, s29, 0
	v_writelane_b32 v254, s2, 32
	s_nop 1
	v_writelane_b32 v254, s3, 33
	s_add_u32 s2, s28, 0x6300000
	v_writelane_b32 v254, s2, 34
	s_addc_u32 s2, s29, 0
	v_writelane_b32 v254, s2, 35
	s_add_u32 s2, s28, 0x1e300000
	v_writelane_b32 v254, s2, 36
	s_addc_u32 s2, s29, 0
	s_add_u32 s36, s28, 0x2a300000
	s_addc_u32 s37, s29, 0
	s_add_u32 s96, s28, 0x36300000
	s_addc_u32 s97, s29, 0
	s_and_b64 s[4:5], s[0:1], s[4:5]
	v_writelane_b32 v254, s2, 37
	s_andn2_b64 vcc, exec, s[4:5]
	s_cbranch_vccnz .LBB0_231
	v_readlane_b32 s1, v254, 3
	s_sub_i32 s0, s1, 46
	s_cmpk_gt_i32 s1, 0x7f
	s_cselect_b32 s2, s0, s1
	s_cmp_lt_i32 s93, s2
	s_cbranch_scc1 .LBB0_77
	v_lshlrev_b32_e32 v146, 2, v0
	s_cbranch_execz .LBB0_78
	s_branch .LBB0_90
